# v43 + out-proj and down K-loops: first iteration peeled with C=0 MFMAs, accumulator zeroing (between the prologue wait and its barrier) removed
# baseline (speedup 1.0000x reference)
; #define PG8_LAS __attribute__((address_space(3)))
;     __device__ __forceinline__ void a_ready(const Unit&) const { if (++ncall == 3 && sig != nullptr && threadIdx.x == 0) __hip_atomic_fetch_add(sig, 1u, __ATOMIC_RELAXED, __HIP_MEMORY_SCOPE_AGENT); }
; __device__ __forceinline__ f32x4 load_row_partials(const float* rsp, int pm, int tid) { f32x4 p = {0.f, 0.f, 0.f, 0.f}; if (tid < BM) p = *(const f32x4*)(rsp + (size_t)(pm * BM + tid) * 4); return p; }
; #define PG8_STAGE(bufoff, gbase, voff) do { _Pragma("unroll") for (int _i = 0; _i < 2; ++_i) \
;         __builtin_amdgcn_global_load_lds((const unsigned*)((const char*)(gbase) + (voff)[_i]), (PG8_LAS unsigned*)(lds + (bufoff) + ldsw + _i * 8192), 16, 0, 0); } while (0)
; #define PG8_WAIT_V(n) asm volatile("s_waitcnt vmcnt(" #n ")" ::: "memory")
; #define PG8_BAR __builtin_amdgcn_s_barrier()
; template <class Epi, class Sched, bool ALIGN_EPI = false, bool SP2 = false>
; __device__ __forceinline__ void gemm_phase(PG8_LAS unsigned char* lds, const Gemm g, const Sched& S, const Epi& E) {
;     ...
;     f32x4 rowp_ = {0.f, 0.f, 0.f, 0.f}; if constexpr (Epi::ROWSCALE) rowp_ = load_row_partials(E.rsp, cur.pm, tid);
;     f32x4 acc[2][2][4][2];
; #pragma unroll
;     for (int a = 0; a < 2; ++a)
; #pragma unroll
;         for (int b = 0; b < 2; ++b)
; #pragma unroll
;             for (int m = 0; m < 4; ++m)
; #pragma unroll
;                 for (int n = 0; n < 2; ++n) acc[a][b][m][n] = (f32x4){0.f, 0.f, 0.f, 0.f};
;     bf16x8 At[4][2], B0[2][2], B1[2][2];
;     const char* cA = (const char*)g.A + (size_t)cur.pm * tstep + (cur.half == 2 ? hstep : (size_t)0); const char* cB = (const char*)g.Bt + (size_t)cur.pn * tstep;
;     S.a_ready(cur);
;     if constexpr (SP2) {
;         PG8_STAGE(PG8_SB(0, 0), cB, voffB); PG8_STAGE(PG8_SB(0, 1), cB + hstep, voffB); PG8_STAGE(PG8_SA(0, 0), cA, voffA); PG8_STAGE(PG8_SA(0, 1), cA + hstep, voffA);
;         if (wr == 1) PG8_BAR;
;         PG8_WAIT_V(2); PG8_BAR;
;         if constexpr (Epi::ROWSCALE) stage_row_factors(rowp_, (PG8_LAS float*)E.rsl, tid);
;         PG8_STAGE(PG8_SB(1, 0), cB + kstep, voffB); PG8_STAGE(PG8_SA(1, 0), cA + kstep, voffA); PG8_STAGE(PG8_SB(1, 1), cB + hstep + kstep, voffB);
;         PG8_WAIT_V(6); PG8_BAR;
.LBB0_1292:
	v_lshl_add_u64 v[10:11], s[0:1], 0, v[2:3]
	v_mov_b32_e32 v137, v3
	v_and_b32_e32 v147, 15, v146
	v_and_b32_e32 v18, 48, v146
	v_lshlrev_b32_e32 v19, 2, v146
	v_lshl_add_u64 v[12:13], s[0:1], 0, v[136:137]
	v_mov_b32_e32 v133, v3
	s_sext_i32_i8 s16, s6
	s_and_b32 s23, s17, 3
	s_lshl_b32 s6, s22, 13
	v_lshl_or_b32 v18, v147, 6, v18
	v_and_b32_e32 v19, 32, v19
	s_add_i32 m0, s40, 0x18000
	v_lshl_add_u64 v[10:11], v[10:11], 0, s[42:43]
	v_lshl_add_u64 v[14:15], s[4:5], 0, v[132:133]
	v_mov_b32_e32 v135, v3
	s_lshl_b32 s9, s22, 6
	v_bitop3_b32 v20, v18, s6, v19 bitop3:0xde
	s_lshl_b32 s6, s23, 12
	s_waitcnt vmcnt(2)
	s_barrier
	global_load_lds_dwordx4 v[10:11], off
	v_lshl_add_u64 v[10:11], v[12:13], 0, s[42:43]
	s_add_i32 m0, s40, 0x1a000
	s_add_i32 s58, s40, 0x8000
	s_add_i32 s59, s40, 0xa000
	v_lshl_add_u64 v[16:17], s[4:5], 0, v[134:135]
	v_bitop3_b32 v148, v18, s6, v19 bitop3:0xde
	global_load_lds_dwordx4 v[10:11], off
	v_lshl_add_u64 v[10:11], v[14:15], 0, s[42:43]
	s_mov_b32 m0, s58
	s_add_u32 s6, s0, 0x40080
	global_load_lds_dwordx4 v[10:11], off
	v_lshl_add_u64 v[10:11], v[16:17], 0, s[42:43]
	s_mov_b32 m0, s59
	s_addc_u32 s7, s1, 0
	global_load_lds_dwordx4 v[10:11], off
	s_add_i32 m0, s40, 0x1c000
	v_lshl_add_u64 v[10:11], s[6:7], 0, v[2:3]
	global_load_lds_dwordx4 v[10:11], off
	v_lshl_add_u64 v[10:11], s[6:7], 0, v[136:137]
	s_add_i32 m0, s40, 0x1e000
	v_or_b32_e32 v214, s9, v147
	global_load_lds_dwordx4 v[10:11], off
	v_lshlrev_b32_e32 v10, 14, v4
	v_and_b32_e32 v10, 0xffff8000, v10
	v_lshl_add_u32 v5, v5, 11, v10
	v_and_b32_e32 v4, 1, v4
	v_lshl_or_b32 v4, v4, 6, v5
	v_lshl_add_u32 v138, v6, 1, v4
	v_lshlrev_b32_e32 v4, 14, v7
	v_and_b32_e32 v4, 0xffff8000, v4
	v_lshl_add_u32 v4, v8, 11, v4
	v_and_b32_e32 v5, 1, v7
	s_waitcnt vmcnt(6)
	v_lshl_or_b32 v4, v5, 6, v4
	v_lshl_add_u32 v140, v9, 1, v4
	v_mov_b32_e32 v139, v3
	v_mov_b32_e32 v141, v3
	s_mov_b32 s60, 0
	v_add_u32_e32 v149, 0, v20
	s_waitcnt lgkmcnt(0)
	s_barrier

;     __device__ bool next(int i, Unit& u) const { if (!base.next(i >> 1, u)) return false; if (i & 1) { u.pm += MTOK / BM; u.pn += DM / BM; } return true; }
; template <class Epi, class Sched, bool ALIGN_EPI = false, bool SP2 = false>
; __device__ __forceinline__ void gemm_phase(PG8_LAS unsigned char* lds, const Gemm g, const Sched& S, const Epi& E) {
;     ...
;     for (;;) {
;         const bool has_next = S.next(ui + 1, nxt);
;         const char* nA = has_next ? (const char*)g.A + (size_t)nxt.pm * tstep + (nxt.half == 2 ? hstep : (size_t)0) : cA; const char* nB = has_next ? (const char*)g.Bt + (size_t)nxt.pn * tstep : cB;
;         for (int t = 0; t < nt; t += 2) {
;             const bool last = (t == nt - 2);
;             const char* a1 = cA + (size_t)(t + 1) * kstep;
;             const char* a2 = last ? nA : cA + (size_t)(t + 2) * kstep; const char* b2 = last ? nB : cB + (size_t)(t + 2) * kstep;
;             const char* a3 = a2 + kstep; const char* b3 = b2 + kstep;
;             if (last && has_next) S.a_ready(nxt);
;             if constexpr (SP2) {
;             PG8_LDB(B0, 0, 0); PG8_LDB(B1, 0, 1); PG8_SCHED; PG8_LDA(At, 0, 0); PG8_STAGE(PG8_SA(1, 1), a1 + hstep, voffA);
;     ...
;             if (PROBE_KIND == 18 && t == 0 && ui > 0 && g.probe) { const unsigned long long tq_ = __builtin_amdgcn_s_memrealtime(); PG8_WAIT_V(8); pg8_probe_acc += (unsigned)(__builtin_amdgcn_s_memrealtime() - tq_); }
;     ...
;             PG8_WAIT_V(8); PG8_WAIT_L(0); PG8_BAR; PG8_MMA(0, 0, At, B0); PG8_MMA(0, 1, At, B1); PG8_BAR; PG8_SCHED;
;             PG8_LDA(At, 0, 1); PG8_STAGE(PG8_SB(0, 0), b2, voffB); PG8_STAGE(PG8_SB(0, 1), b2 + hstep, voffB); PG8_STAGE(PG8_SA(0, 0), a2, voffA);
;             PG8_WAIT_V(8); PG8_WAIT_L(0); PG8_BAR; if (cur.half == 0) { PG8_MMA(1, 0, At, B0); PG8_MMA(1, 1, At, B1); } PG8_BAR; PG8_SCHED;
;             PG8_LDB(B0, 1, 0); PG8_LDB(B1, 1, 1); PG8_SCHED; PG8_LDA(At, 1, 0); PG8_STAGE(PG8_SA(0, 1), a2 + hstep, voffA);
;             PG8_WAIT_V(8); PG8_WAIT_L(0); PG8_BAR; PG8_MMA(0, 0, At, B0); PG8_MMA(0, 1, At, B1); PG8_BAR; PG8_SCHED;
;             PG8_LDA(At, 1, 1); PG8_STAGE(PG8_SB(1, 0), b3, voffB); PG8_STAGE(PG8_SB(1, 1), b3 + hstep, voffB); PG8_STAGE(PG8_SA(1, 0), a3, voffA);
;             PG8_WAIT_V(8); PG8_WAIT_L(0); PG8_BAR; if (cur.half == 0) { PG8_MMA(1, 0, At, B0); PG8_MMA(1, 1, At, B1); } PG8_BAR; PG8_SCHED;
.LBB0_1299:
	s_add_u32 s62, s0, 0x100
	s_addc_u32 s63, s1, 0
	s_ashr_i32 s7, s6, 31
	s_lshl_b64 s[18:19], s[6:7], 19
	s_add_u32 s26, s34, s18
	s_addc_u32 s27, s35, s19
	s_and_b64 s[18:19], s[20:21], exec
	s_cselect_b32 s7, s27, s5
	s_cselect_b32 s64, s26, s4
	s_ashr_i32 s11, s10, 31
	s_lshl_b64 s[18:19], s[10:11], 19
	s_add_u32 s18, s36, s18
	s_addc_u32 s19, s38, s19
	s_and_b64 s[28:29], s[20:21], exec
	s_cselect_b32 s11, s19, s1
	s_cselect_b32 s65, s18, s0
	s_add_u32 s0, s4, 0x40080
	s_addc_u32 s1, s5, 0
	v_lshl_add_u64 v[142:143], s[0:1], 0, v[138:139]
	v_lshl_add_u64 v[144:145], s[0:1], 0, v[140:141]
	s_mov_b32 s66, -2
	s_mov_b64 s[0:1], 0
	s_add_u32 s28, s4, s0
	s_addc_u32 s29, s5, s1
	s_add_u32 s28, s28, 0x100
	s_addc_u32 s29, s29, 0
	s_add_u32 s67, s62, s0
	s_addc_u32 s68, s63, s1
	s_add_i32 s69, 0, 0x10000
	s_cmpk_eq_i32 s0, 0x700
	s_cselect_b32 s31, s7, s29
	s_cselect_b32 s30, s64, s28
	s_cselect_b32 s29, s11, s68
	s_cselect_b32 s28, s65, s67
	s_add_i32 s67, 0, 0x14000
	v_add_u32_e32 v162, s69, v148
	v_add_u32_e32 v178, s67, v148
	ds_read_b128 v[150:153], v162
	ds_read_b128 v[154:157], v162 offset:1024
	ds_read_b128 v[158:161], v162 offset:2048
	ds_read_b128 v[162:165], v162 offset:3072
	ds_read_b128 v[166:169], v178
	ds_read_b128 v[170:173], v178 offset:1024
	ds_read_b128 v[174:177], v178 offset:2048
	ds_read_b128 v[178:181], v178 offset:3072
	v_lshl_add_u64 v[216:217], v[142:143], 0, s[0:1]
	s_add_i32 m0, s40, 0xc000
	ds_read_b128 v[182:185], v149
	ds_read_b128 v[186:189], v149 offset:1024
	ds_read_b128 v[190:193], v149 offset:2048
	ds_read_b128 v[194:197], v149 offset:3072
	ds_read_b128 v[198:201], v149 offset:4096
	ds_read_b128 v[202:205], v149 offset:5120
	ds_read_b128 v[206:209], v149 offset:6144
	ds_read_b128 v[210:213], v149 offset:7168
	global_load_lds_dwordx4 v[216:217], off
	v_lshl_add_u64 v[216:217], v[144:145], 0, s[0:1]
	s_add_i32 m0, s40, 0xe000
	s_nop 0
	global_load_lds_dwordx4 v[216:217], off
	s_waitcnt vmcnt(8)
	s_waitcnt lgkmcnt(0)
	s_barrier
	s_setprio 1
	s_waitcnt lgkmcnt(0)
	v_mfma_f32_16x16x32_bf16 v[128:131], v[150:153], v[182:185], 0
	v_mfma_f32_16x16x32_bf16 v[124:127], v[158:161], v[182:185], 0
	v_mfma_f32_16x16x32_bf16 v[112:115], v[150:153], v[190:193], 0
	v_mfma_f32_16x16x32_bf16 v[108:111], v[158:161], v[190:193], 0
	v_mfma_f32_16x16x32_bf16 v[96:99], v[150:153], v[198:201], 0
	v_mfma_f32_16x16x32_bf16 v[92:95], v[158:161], v[198:201], 0
	v_mfma_f32_16x16x32_bf16 v[80:83], v[150:153], v[206:209], 0
	v_mfma_f32_16x16x32_bf16 v[76:79], v[158:161], v[206:209], 0
	v_mfma_f32_16x16x32_bf16 v[128:131], v[154:157], v[186:189], v[128:131]
	v_mfma_f32_16x16x32_bf16 v[124:127], v[162:165], v[186:189], v[124:127]
	v_mfma_f32_16x16x32_bf16 v[112:115], v[154:157], v[194:197], v[112:115]
	v_mfma_f32_16x16x32_bf16 v[108:111], v[162:165], v[194:197], v[108:111]
	v_mfma_f32_16x16x32_bf16 v[96:99], v[154:157], v[202:205], v[96:99]
	v_mfma_f32_16x16x32_bf16 v[92:95], v[162:165], v[202:205], v[92:95]
	v_mfma_f32_16x16x32_bf16 v[80:83], v[154:157], v[210:213], v[80:83]
	v_mfma_f32_16x16x32_bf16 v[76:79], v[162:165], v[210:213], v[76:79]
	s_setprio 0
	s_setprio 1
	v_mfma_f32_16x16x32_bf16 v[120:123], v[166:169], v[182:185], 0
	v_mfma_f32_16x16x32_bf16 v[116:119], v[174:177], v[182:185], 0
	v_mfma_f32_16x16x32_bf16 v[104:107], v[166:169], v[190:193], 0
	v_mfma_f32_16x16x32_bf16 v[100:103], v[174:177], v[190:193], 0
	v_mfma_f32_16x16x32_bf16 v[88:91], v[166:169], v[198:201], 0
	v_mfma_f32_16x16x32_bf16 v[84:87], v[174:177], v[198:201], 0
	v_mfma_f32_16x16x32_bf16 v[72:75], v[166:169], v[206:209], 0
	v_mfma_f32_16x16x32_bf16 v[68:71], v[174:177], v[206:209], 0
	v_mfma_f32_16x16x32_bf16 v[120:123], v[170:173], v[186:189], v[120:123]
	v_mfma_f32_16x16x32_bf16 v[116:119], v[178:181], v[186:189], v[116:119]
	v_mfma_f32_16x16x32_bf16 v[104:107], v[170:173], v[194:197], v[104:107]
	v_mfma_f32_16x16x32_bf16 v[100:103], v[178:181], v[194:197], v[100:103]
	v_mfma_f32_16x16x32_bf16 v[88:91], v[170:173], v[202:205], v[88:91]
	v_mfma_f32_16x16x32_bf16 v[84:87], v[178:181], v[202:205], v[84:87]
	v_mfma_f32_16x16x32_bf16 v[72:75], v[170:173], v[210:213], v[72:75]
	v_mfma_f32_16x16x32_bf16 v[68:71], v[178:181], v[210:213], v[68:71]
	s_setprio 0
	s_barrier
	s_add_i32 s68, s69, s39
	v_lshl_add_u64 v[216:217], s[28:29], 0, v[2:3]
	s_mov_b32 m0, s68
	ds_read_b128 v[182:185], v149 offset:16384
	ds_read_b128 v[186:189], v149 offset:17408
	ds_read_b128 v[190:193], v149 offset:18432
	ds_read_b128 v[194:197], v149 offset:19456
	ds_read_b128 v[198:201], v149 offset:20480
	ds_read_b128 v[202:205], v149 offset:21504
	ds_read_b128 v[206:209], v149 offset:22528
	ds_read_b128 v[210:213], v149 offset:23552
	global_load_lds_dwordx4 v[216:217], off
	s_add_i32 m0, s68, 0x2000
	s_add_u32 s68, s28, 0x40000
	v_lshl_add_u64 v[218:219], s[28:29], 0, v[136:137]
	s_addc_u32 s69, s29, 0
	s_add_i32 s67, s67, s39
	global_load_lds_dwordx4 v[218:219], off
	v_lshl_add_u64 v[220:221], s[68:69], 0, v[2:3]
	s_mov_b32 m0, s67
	v_lshl_add_u64 v[228:229], s[30:31], 0, v[134:135]
	global_load_lds_dwordx4 v[220:221], off
	v_lshl_add_u64 v[220:221], s[68:69], 0, v[136:137]
	s_add_i32 m0, s67, 0x2000
	s_nop 0
	global_load_lds_dwordx4 v[220:221], off
	v_lshl_add_u64 v[220:221], s[30:31], 0, v[132:133]
	s_mov_b32 m0, s40
	s_nop 0
	global_load_lds_dwordx4 v[220:221], off
	s_mov_b32 m0, s41
	s_nop 0
	global_load_lds_dwordx4 v[228:229], off
	s_waitcnt vmcnt(8)
	s_waitcnt lgkmcnt(0)
	s_barrier
; #define PG8_STAGE(bufoff, gbase, voff) do { _Pragma("unroll") for (int _i = 0; _i < 2; ++_i) \
;         __builtin_amdgcn_global_load_lds((const unsigned*)((const char*)(gbase) + (voff)[_i]), (PG8_LAS unsigned*)(lds + (bufoff) + ldsw + _i * 8192), 16, 0, 0); } while (0)
; #define PG8_LDA(dst, b, h) do { _Pragma("unroll") for (int m = 0; m < 4; ++m) _Pragma("unroll") for (int k = 0; k < 2; ++k) dst[m][k] = *(const PG8_LAS bf16x8*)(lds + PG8_SA(b, h) + aoff + m * 2048 + k * 1024); } while (0)
; #define PG8_LDB(dst, b, h) do { _Pragma("unroll") for (int n = 0; n < 2; ++n) _Pragma("unroll") for (int k = 0; k < 2; ++k) dst[n][k] = *(const PG8_LAS bf16x8*)(lds + PG8_SB(b, h) + boff + n * 2048 + k * 1024); } while (0)
; #define PG8_WAIT_V(n) asm volatile("s_waitcnt vmcnt(" #n ")" ::: "memory")
; #define PG8_WAIT_L(n) asm volatile("s_waitcnt lgkmcnt(" #n ")" ::: "memory")
; template <class Epi, class Sched, bool ALIGN_EPI = false, bool SP2 = false>
; __device__ __forceinline__ void gemm_phase(PG8_LAS unsigned char* lds, const Gemm g, const Sched& S, const Epi& E) {
;     ...
;             PG8_LDB(B0, 0, 0); PG8_LDB(B1, 0, 1); PG8_SCHED; PG8_LDA(At, 0, 0); PG8_STAGE(PG8_SA(1, 1), a1 + hstep, voffA);
;     ...
;             if (PROBE_KIND == 18 && t == 0 && ui > 0 && g.probe) { const unsigned long long tq_ = __builtin_amdgcn_s_memrealtime(); PG8_WAIT_V(8); pg8_probe_acc += (unsigned)(__builtin_amdgcn_s_memrealtime() - tq_); }
;     ...
;             PG8_WAIT_V(8); PG8_WAIT_L(0); PG8_BAR; PG8_MMA(0, 0, At, B0); PG8_MMA(0, 1, At, B1); PG8_BAR; PG8_SCHED;
;             PG8_LDA(At, 0, 1); PG8_STAGE(PG8_SB(0, 0), b2, voffB); PG8_STAGE(PG8_SB(0, 1), b2 + hstep, voffB); PG8_STAGE(PG8_SA(0, 0), a2, voffA);
;             PG8_WAIT_V(8); PG8_WAIT_L(0); PG8_BAR; if (cur.half == 0) { PG8_MMA(1, 0, At, B0); PG8_MMA(1, 1, At, B1); } PG8_BAR; PG8_SCHED;
;             PG8_LDB(B0, 1, 0); PG8_LDB(B1, 1, 1); PG8_SCHED; PG8_LDA(At, 1, 0); PG8_STAGE(PG8_SA(0, 1), a2 + hstep, voffA);
;             PG8_WAIT_V(8); PG8_WAIT_L(0); PG8_BAR; PG8_MMA(0, 0, At, B0); PG8_MMA(0, 1, At, B1); PG8_BAR; PG8_SCHED;
;             PG8_LDA(At, 1, 1); PG8_STAGE(PG8_SB(1, 0), b3, voffB); PG8_STAGE(PG8_SB(1, 1), b3 + hstep, voffB); PG8_STAGE(PG8_SA(1, 0), a3, voffA);
;             PG8_WAIT_V(8); PG8_WAIT_L(0); PG8_BAR; if (cur.half == 0) { PG8_MMA(1, 0, At, B0); PG8_MMA(1, 1, At, B1); } PG8_BAR; PG8_SCHED;
	s_setprio 1
	s_waitcnt lgkmcnt(0)
	v_mfma_f32_16x16x32_bf16 v[64:67], v[150:153], v[182:185], 0
	v_mfma_f32_16x16x32_bf16 v[60:63], v[158:161], v[182:185], 0
	v_mfma_f32_16x16x32_bf16 v[48:51], v[150:153], v[190:193], 0
	v_mfma_f32_16x16x32_bf16 v[44:47], v[158:161], v[190:193], 0
	v_mfma_f32_16x16x32_bf16 v[32:35], v[150:153], v[198:201], 0
	v_mfma_f32_16x16x32_bf16 v[28:31], v[158:161], v[198:201], 0
	v_mfma_f32_16x16x32_bf16 v[16:19], v[150:153], v[206:209], 0
	v_mfma_f32_16x16x32_bf16 v[12:15], v[158:161], v[206:209], 0
	v_mfma_f32_16x16x32_bf16 v[64:67], v[154:157], v[186:189], v[64:67]
	v_mfma_f32_16x16x32_bf16 v[60:63], v[162:165], v[186:189], v[60:63]
	v_mfma_f32_16x16x32_bf16 v[48:51], v[154:157], v[194:197], v[48:51]
	v_mfma_f32_16x16x32_bf16 v[44:47], v[162:165], v[194:197], v[44:47]
	v_mfma_f32_16x16x32_bf16 v[32:35], v[154:157], v[202:205], v[32:35]
	v_mfma_f32_16x16x32_bf16 v[28:31], v[162:165], v[202:205], v[28:31]
	v_mfma_f32_16x16x32_bf16 v[16:19], v[154:157], v[210:213], v[16:19]
	v_mfma_f32_16x16x32_bf16 v[12:15], v[162:165], v[210:213], v[12:15]
	s_setprio 0
	s_setprio 1
	v_mfma_f32_16x16x32_bf16 v[56:59], v[166:169], v[182:185], 0
	v_mfma_f32_16x16x32_bf16 v[52:55], v[174:177], v[182:185], 0
	v_mfma_f32_16x16x32_bf16 v[40:43], v[166:169], v[190:193], 0
	v_mfma_f32_16x16x32_bf16 v[36:39], v[174:177], v[190:193], 0
	v_mfma_f32_16x16x32_bf16 v[24:27], v[166:169], v[198:201], 0
	v_mfma_f32_16x16x32_bf16 v[20:23], v[174:177], v[198:201], 0
	v_mfma_f32_16x16x32_bf16 v[8:11], v[166:169], v[206:209], 0
	v_mfma_f32_16x16x32_bf16 v[4:7], v[174:177], v[206:209], 0
	v_mfma_f32_16x16x32_bf16 v[56:59], v[170:173], v[186:189], v[56:59]
	v_mfma_f32_16x16x32_bf16 v[52:55], v[178:181], v[186:189], v[52:55]
	v_mfma_f32_16x16x32_bf16 v[40:43], v[170:173], v[194:197], v[40:43]
	v_mfma_f32_16x16x32_bf16 v[36:39], v[178:181], v[194:197], v[36:39]
	v_mfma_f32_16x16x32_bf16 v[24:27], v[170:173], v[202:205], v[24:27]
	v_mfma_f32_16x16x32_bf16 v[20:23], v[178:181], v[202:205], v[20:23]
	v_mfma_f32_16x16x32_bf16 v[8:11], v[170:173], v[210:213], v[8:11]
	v_mfma_f32_16x16x32_bf16 v[4:7], v[178:181], v[210:213], v[4:7]
	s_setprio 0
	s_barrier
	s_add_i32 s67, 0, 0x18000
	s_add_i32 s68, 0, 0x1c000
	v_add_u32_e32 v162, s67, v148
	v_add_u32_e32 v178, s68, v148
	ds_read_b128 v[150:153], v162
	ds_read_b128 v[154:157], v162 offset:1024
	ds_read_b128 v[158:161], v162 offset:2048
	ds_read_b128 v[162:165], v162 offset:3072
	ds_read_b128 v[166:169], v178
	ds_read_b128 v[170:173], v178 offset:1024
	ds_read_b128 v[174:177], v178 offset:2048
	ds_read_b128 v[178:181], v178 offset:3072
	s_add_u32 s30, s30, 0x40000
	s_addc_u32 s31, s31, 0
	s_mov_b32 m0, s56
	v_lshl_add_u64 v[230:231], s[30:31], 0, v[132:133]
	ds_read_b128 v[182:185], v149 offset:32768
	ds_read_b128 v[186:189], v149 offset:33792
	ds_read_b128 v[190:193], v149 offset:34816
	ds_read_b128 v[194:197], v149 offset:35840
	ds_read_b128 v[198:201], v149 offset:36864
	ds_read_b128 v[202:205], v149 offset:37888
	ds_read_b128 v[206:209], v149 offset:38912
	ds_read_b128 v[210:213], v149 offset:39936
	global_load_lds_dwordx4 v[230:231], off
	v_lshl_add_u64 v[230:231], s[30:31], 0, v[134:135]
	s_mov_b32 m0, s57
	s_nop 0
	global_load_lds_dwordx4 v[230:231], off
	s_waitcnt vmcnt(8)
	s_waitcnt lgkmcnt(0)
	s_barrier
	s_setprio 1
	s_waitcnt lgkmcnt(0)
	v_mfma_f32_16x16x32_bf16 v[128:131], v[150:153], v[182:185], v[128:131]
	v_mfma_f32_16x16x32_bf16 v[124:127], v[158:161], v[182:185], v[124:127]
	v_mfma_f32_16x16x32_bf16 v[112:115], v[150:153], v[190:193], v[112:115]
	v_mfma_f32_16x16x32_bf16 v[108:111], v[158:161], v[190:193], v[108:111]
	v_mfma_f32_16x16x32_bf16 v[96:99], v[150:153], v[198:201], v[96:99]
	v_mfma_f32_16x16x32_bf16 v[92:95], v[158:161], v[198:201], v[92:95]
	v_mfma_f32_16x16x32_bf16 v[80:83], v[150:153], v[206:209], v[80:83]
	v_mfma_f32_16x16x32_bf16 v[76:79], v[158:161], v[206:209], v[76:79]
	v_mfma_f32_16x16x32_bf16 v[128:131], v[154:157], v[186:189], v[128:131]
	v_mfma_f32_16x16x32_bf16 v[124:127], v[162:165], v[186:189], v[124:127]
	v_mfma_f32_16x16x32_bf16 v[112:115], v[154:157], v[194:197], v[112:115]
	v_mfma_f32_16x16x32_bf16 v[108:111], v[162:165], v[194:197], v[108:111]
	v_mfma_f32_16x16x32_bf16 v[96:99], v[154:157], v[202:205], v[96:99]
	v_mfma_f32_16x16x32_bf16 v[92:95], v[162:165], v[202:205], v[92:95]
	v_mfma_f32_16x16x32_bf16 v[80:83], v[154:157], v[210:213], v[80:83]
	v_mfma_f32_16x16x32_bf16 v[76:79], v[162:165], v[210:213], v[76:79]
	s_setprio 0
	s_setprio 1
	v_mfma_f32_16x16x32_bf16 v[120:123], v[166:169], v[182:185], v[120:123]
	v_mfma_f32_16x16x32_bf16 v[116:119], v[174:177], v[182:185], v[116:119]
	v_mfma_f32_16x16x32_bf16 v[104:107], v[166:169], v[190:193], v[104:107]
	v_mfma_f32_16x16x32_bf16 v[100:103], v[174:177], v[190:193], v[100:103]
	v_mfma_f32_16x16x32_bf16 v[88:91], v[166:169], v[198:201], v[88:91]
	v_mfma_f32_16x16x32_bf16 v[84:87], v[174:177], v[198:201], v[84:87]
	v_mfma_f32_16x16x32_bf16 v[72:75], v[166:169], v[206:209], v[72:75]
	v_mfma_f32_16x16x32_bf16 v[68:71], v[174:177], v[206:209], v[68:71]
	v_mfma_f32_16x16x32_bf16 v[120:123], v[170:173], v[186:189], v[120:123]
	v_mfma_f32_16x16x32_bf16 v[116:119], v[178:181], v[186:189], v[116:119]
	v_mfma_f32_16x16x32_bf16 v[104:107], v[170:173], v[194:197], v[104:107]
	v_mfma_f32_16x16x32_bf16 v[100:103], v[178:181], v[194:197], v[100:103]
	v_mfma_f32_16x16x32_bf16 v[88:91], v[170:173], v[202:205], v[88:91]
	v_mfma_f32_16x16x32_bf16 v[84:87], v[178:181], v[202:205], v[84:87]
	v_mfma_f32_16x16x32_bf16 v[72:75], v[170:173], v[210:213], v[72:75]
	v_mfma_f32_16x16x32_bf16 v[68:71], v[178:181], v[210:213], v[68:71]
	s_setprio 0
	s_barrier
; #define PG8_STAGE(bufoff, gbase, voff) do { _Pragma("unroll") for (int _i = 0; _i < 2; ++_i) \
;         __builtin_amdgcn_global_load_lds((const unsigned*)((const char*)(gbase) + (voff)[_i]), (PG8_LAS unsigned*)(lds + (bufoff) + ldsw + _i * 8192), 16, 0, 0); } while (0)
; #define PG8_LDA(dst, b, h) do { _Pragma("unroll") for (int m = 0; m < 4; ++m) _Pragma("unroll") for (int k = 0; k < 2; ++k) dst[m][k] = *(const PG8_LAS bf16x8*)(lds + PG8_SA(b, h) + aoff + m * 2048 + k * 1024); } while (0)
; #define PG8_LDB(dst, b, h) do { _Pragma("unroll") for (int n = 0; n < 2; ++n) _Pragma("unroll") for (int k = 0; k < 2; ++k) dst[n][k] = *(const PG8_LAS bf16x8*)(lds + PG8_SB(b, h) + boff + n * 2048 + k * 1024); } while (0)
; #define PG8_WAIT_V(n) asm volatile("s_waitcnt vmcnt(" #n ")" ::: "memory")
; #define PG8_WAIT_L(n) asm volatile("s_waitcnt lgkmcnt(" #n ")" ::: "memory")
; template <class Epi, class Sched, bool ALIGN_EPI = false, bool SP2 = false>
; __device__ __forceinline__ void gemm_phase(PG8_LAS unsigned char* lds, const Gemm g, const Sched& S, const Epi& E) {
;     ...
;             PG8_LDB(B0, 0, 0); PG8_LDB(B1, 0, 1); PG8_SCHED; PG8_LDA(At, 0, 0); PG8_STAGE(PG8_SA(1, 1), a1 + hstep, voffA);
;     ...
;             if (PROBE_KIND == 18 && t == 0 && ui > 0 && g.probe) { const unsigned long long tq_ = __builtin_amdgcn_s_memrealtime(); PG8_WAIT_V(8); pg8_probe_acc += (unsigned)(__builtin_amdgcn_s_memrealtime() - tq_); }
;     ...
;             PG8_WAIT_V(8); PG8_WAIT_L(0); PG8_BAR; PG8_MMA(0, 0, At, B0); PG8_MMA(0, 1, At, B1); PG8_BAR; PG8_SCHED;
;             PG8_LDA(At, 0, 1); PG8_STAGE(PG8_SB(0, 0), b2, voffB); PG8_STAGE(PG8_SB(0, 1), b2 + hstep, voffB); PG8_STAGE(PG8_SA(0, 0), a2, voffA);
;             PG8_WAIT_V(8); PG8_WAIT_L(0); PG8_BAR; if (cur.half == 0) { PG8_MMA(1, 0, At, B0); PG8_MMA(1, 1, At, B1); } PG8_BAR; PG8_SCHED;
;             PG8_LDB(B0, 1, 0); PG8_LDB(B1, 1, 1); PG8_SCHED; PG8_LDA(At, 1, 0); PG8_STAGE(PG8_SA(0, 1), a2 + hstep, voffA);
;             PG8_WAIT_V(8); PG8_WAIT_L(0); PG8_BAR; PG8_MMA(0, 0, At, B0); PG8_MMA(0, 1, At, B1); PG8_BAR; PG8_SCHED;
;             PG8_LDA(At, 1, 1); PG8_STAGE(PG8_SB(1, 0), b3, voffB); PG8_STAGE(PG8_SB(1, 1), b3 + hstep, voffB); PG8_STAGE(PG8_SA(1, 0), a3, voffA);
;             PG8_WAIT_V(8); PG8_WAIT_L(0); PG8_BAR; if (cur.half == 0) { PG8_MMA(1, 0, At, B0); PG8_MMA(1, 1, At, B1); } PG8_BAR; PG8_SCHED;
	s_add_i32 s30, s67, s39
	v_lshl_add_u64 v[216:217], v[216:217], 0, s[42:43]
	s_mov_b32 m0, s30
	ds_read_b128 v[182:185], v149 offset:49152
	ds_read_b128 v[186:189], v149 offset:50176
	ds_read_b128 v[190:193], v149 offset:51200
	ds_read_b128 v[194:197], v149 offset:52224
	ds_read_b128 v[198:201], v149 offset:53248
	ds_read_b128 v[202:205], v149 offset:54272
	ds_read_b128 v[206:209], v149 offset:55296
	ds_read_b128 v[210:213], v149 offset:56320
	global_load_lds_dwordx4 v[216:217], off
	s_add_i32 m0, s30, 0x2000
	s_add_u32 s28, s28, 0x40080
	v_lshl_add_u64 v[216:217], v[218:219], 0, s[42:43]
	s_addc_u32 s29, s29, 0
	s_add_i32 s30, s68, s39
	global_load_lds_dwordx4 v[216:217], off
	v_lshl_add_u64 v[216:217], s[28:29], 0, v[2:3]
	s_mov_b32 m0, s30
	s_nop 0
	global_load_lds_dwordx4 v[216:217], off
	v_lshl_add_u64 v[216:217], s[28:29], 0, v[136:137]
	s_add_i32 m0, s30, 0x2000
	s_nop 0
	global_load_lds_dwordx4 v[216:217], off
	v_lshl_add_u64 v[216:217], v[220:221], 0, s[42:43]
	s_mov_b32 m0, s58
	s_nop 0
	global_load_lds_dwordx4 v[216:217], off
	v_lshl_add_u64 v[216:217], v[228:229], 0, s[42:43]
	s_mov_b32 m0, s59
	s_nop 0
	global_load_lds_dwordx4 v[216:217], off
	s_waitcnt vmcnt(8)
	s_waitcnt lgkmcnt(0)
	s_barrier
	s_setprio 1
	s_waitcnt lgkmcnt(0)
	v_mfma_f32_16x16x32_bf16 v[64:67], v[150:153], v[182:185], v[64:67]
	v_mfma_f32_16x16x32_bf16 v[60:63], v[158:161], v[182:185], v[60:63]
	v_mfma_f32_16x16x32_bf16 v[48:51], v[150:153], v[190:193], v[48:51]
	v_mfma_f32_16x16x32_bf16 v[44:47], v[158:161], v[190:193], v[44:47]
	v_mfma_f32_16x16x32_bf16 v[32:35], v[150:153], v[198:201], v[32:35]
	v_mfma_f32_16x16x32_bf16 v[28:31], v[158:161], v[198:201], v[28:31]
	v_mfma_f32_16x16x32_bf16 v[16:19], v[150:153], v[206:209], v[16:19]
	v_mfma_f32_16x16x32_bf16 v[12:15], v[158:161], v[206:209], v[12:15]
	v_mfma_f32_16x16x32_bf16 v[64:67], v[154:157], v[186:189], v[64:67]
	v_mfma_f32_16x16x32_bf16 v[60:63], v[162:165], v[186:189], v[60:63]
	v_mfma_f32_16x16x32_bf16 v[48:51], v[154:157], v[194:197], v[48:51]
	v_mfma_f32_16x16x32_bf16 v[44:47], v[162:165], v[194:197], v[44:47]
	v_mfma_f32_16x16x32_bf16 v[32:35], v[154:157], v[202:205], v[32:35]
	v_mfma_f32_16x16x32_bf16 v[28:31], v[162:165], v[202:205], v[28:31]
	v_mfma_f32_16x16x32_bf16 v[16:19], v[154:157], v[210:213], v[16:19]
	v_mfma_f32_16x16x32_bf16 v[12:15], v[162:165], v[210:213], v[12:15]
	s_setprio 0
	s_setprio 1
	v_mfma_f32_16x16x32_bf16 v[56:59], v[166:169], v[182:185], v[56:59]
	v_mfma_f32_16x16x32_bf16 v[52:55], v[174:177], v[182:185], v[52:55]
	v_mfma_f32_16x16x32_bf16 v[40:43], v[166:169], v[190:193], v[40:43]
	v_mfma_f32_16x16x32_bf16 v[36:39], v[174:177], v[190:193], v[36:39]
	v_mfma_f32_16x16x32_bf16 v[24:27], v[166:169], v[198:201], v[24:27]
	v_mfma_f32_16x16x32_bf16 v[20:23], v[174:177], v[198:201], v[20:23]
	v_mfma_f32_16x16x32_bf16 v[8:11], v[166:169], v[206:209], v[8:11]
	v_mfma_f32_16x16x32_bf16 v[4:7], v[174:177], v[206:209], v[4:7]
	v_mfma_f32_16x16x32_bf16 v[56:59], v[170:173], v[186:189], v[56:59]
	v_mfma_f32_16x16x32_bf16 v[52:55], v[178:181], v[186:189], v[52:55]
	v_mfma_f32_16x16x32_bf16 v[40:43], v[170:173], v[194:197], v[40:43]
	v_mfma_f32_16x16x32_bf16 v[36:39], v[178:181], v[194:197], v[36:39]
	v_mfma_f32_16x16x32_bf16 v[24:27], v[170:173], v[202:205], v[24:27]
	v_mfma_f32_16x16x32_bf16 v[20:23], v[178:181], v[202:205], v[20:23]
	v_mfma_f32_16x16x32_bf16 v[8:11], v[170:173], v[210:213], v[8:11]
	v_mfma_f32_16x16x32_bf16 v[4:7], v[178:181], v[210:213], v[4:7]
	s_setprio 0
	s_barrier
	s_add_i32 s66, s66, 2
	s_add_u32 s0, s0, 0x100
	s_addc_u32 s1, s1, 0

; #define PG8_LAS __attribute__((address_space(3)))
;     __device__ __forceinline__ void a_ready(const Unit&) const { if (++ncall == 3 && sig != nullptr && threadIdx.x == 0) __hip_atomic_fetch_add(sig, 1u, __ATOMIC_RELAXED, __HIP_MEMORY_SCOPE_AGENT); }
; __device__ __forceinline__ f32x4 load_row_partials(const float* rsp, int pm, int tid) { f32x4 p = {0.f, 0.f, 0.f, 0.f}; if (tid < BM) p = *(const f32x4*)(rsp + (size_t)(pm * BM + tid) * 4); return p; }
; #define PG8_STAGE(bufoff, gbase, voff) do { _Pragma("unroll") for (int _i = 0; _i < 2; ++_i) \
;         __builtin_amdgcn_global_load_lds((const unsigned*)((const char*)(gbase) + (voff)[_i]), (PG8_LAS unsigned*)(lds + (bufoff) + ldsw + _i * 8192), 16, 0, 0); } while (0)
; #define PG8_WAIT_V(n) asm volatile("s_waitcnt vmcnt(" #n ")" ::: "memory")
; #define PG8_BAR __builtin_amdgcn_s_barrier()
; template <class Epi, class Sched, bool ALIGN_EPI = false, bool SP2 = false>
; __device__ __forceinline__ void gemm_phase(PG8_LAS unsigned char* lds, const Gemm g, const Sched& S, const Epi& E) {
;     ...
;     f32x4 rowp_ = {0.f, 0.f, 0.f, 0.f}; if constexpr (Epi::ROWSCALE) rowp_ = load_row_partials(E.rsp, cur.pm, tid);
;     f32x4 acc[2][2][4][2];
; #pragma unroll
;     for (int a = 0; a < 2; ++a)
; #pragma unroll
;         for (int b = 0; b < 2; ++b)
; #pragma unroll
;             for (int m = 0; m < 4; ++m)
; #pragma unroll
;                 for (int n = 0; n < 2; ++n) acc[a][b][m][n] = (f32x4){0.f, 0.f, 0.f, 0.f};
;     bf16x8 At[4][2], B0[2][2], B1[2][2];
;     const char* cA = (const char*)g.A + (size_t)cur.pm * tstep + (cur.half == 2 ? hstep : (size_t)0); const char* cB = (const char*)g.Bt + (size_t)cur.pn * tstep;
;     S.a_ready(cur);
;     if constexpr (SP2) {
;         PG8_STAGE(PG8_SB(0, 0), cB, voffB); PG8_STAGE(PG8_SB(0, 1), cB + hstep, voffB); PG8_STAGE(PG8_SA(0, 0), cA, voffA); PG8_STAGE(PG8_SA(0, 1), cA + hstep, voffA);
;         if (wr == 1) PG8_BAR;
;         PG8_WAIT_V(2); PG8_BAR;
;         if constexpr (Epi::ROWSCALE) stage_row_factors(rowp_, (PG8_LAS float*)E.rsl, tid);
;         PG8_STAGE(PG8_SB(1, 0), cB + kstep, voffB); PG8_STAGE(PG8_SA(1, 0), cA + kstep, voffA); PG8_STAGE(PG8_SB(1, 1), cB + hstep + kstep, voffB);
;         PG8_WAIT_V(6); PG8_BAR;
.LBB0_1768:
	s_lshr_b32 s4, s4, 3
	v_lshl_add_u64 v[12:13], s[0:1], 0, v[2:3]
	v_mov_b32_e32 v137, v3
	v_and_b32_e32 v147, 15, v146
	v_and_b32_e32 v20, 48, v146
	v_lshlrev_b32_e32 v21, 2, v146
	v_lshl_add_u64 v[14:15], s[0:1], 0, v[136:137]
	v_mov_b32_e32 v133, v3
	s_sext_i32_i8 s16, s4
	s_and_b32 s25, s17, 3
	s_lshl_b32 s4, s22, 13
	v_lshl_or_b32 v20, v147, 6, v20
	v_and_b32_e32 v21, 32, v21
	s_add_i32 m0, s35, 0x18000
	v_lshl_add_u64 v[12:13], v[12:13], 0, s[42:43]
	v_lshl_add_u64 v[16:17], s[6:7], 0, v[132:133]
	v_mov_b32_e32 v135, v3
	s_lshl_b32 s24, s22, 6
	v_bitop3_b32 v22, v20, s4, v21 bitop3:0xde
	s_lshl_b32 s4, s25, 12
	s_waitcnt vmcnt(2)
	s_barrier
	global_load_lds_dwordx4 v[12:13], off
	v_lshl_add_u64 v[12:13], v[14:15], 0, s[42:43]
	s_add_i32 m0, s35, 0x1a000
	s_add_i32 s40, s35, 0x8000
	s_add_i32 s41, s35, 0xa000
	v_lshl_add_u64 v[18:19], s[6:7], 0, v[134:135]
	v_bitop3_b32 v148, v20, s4, v21 bitop3:0xde
	global_load_lds_dwordx4 v[12:13], off
	v_lshl_add_u64 v[12:13], v[16:17], 0, s[42:43]
	s_mov_b32 m0, s40
	s_add_u32 s4, s0, 0xb0080
	global_load_lds_dwordx4 v[12:13], off
	v_lshl_add_u64 v[12:13], v[18:19], 0, s[42:43]
	s_mov_b32 m0, s41
	s_addc_u32 s5, s1, 0
	global_load_lds_dwordx4 v[12:13], off
	s_add_i32 m0, s35, 0x1c000
	v_lshl_add_u64 v[12:13], s[4:5], 0, v[2:3]
	global_load_lds_dwordx4 v[12:13], off
	v_lshl_add_u64 v[12:13], s[4:5], 0, v[136:137]
	s_add_i32 m0, s35, 0x1e000
	s_movk_i32 s8, 0xb00
	global_load_lds_dwordx4 v[12:13], off
	v_lshrrev_b32_e32 v12, 1, v4
	v_mul_lo_u32 v4, v6, s8
	s_mov_b32 s9, 0xb000
	v_mad_u64_u32 v[12:13], s[4:5], v12, s9, v[4:5]
	v_or_b32_e32 v4, v12, v5
	v_add_lshl_u32 v138, v4, v7, 1
	v_lshrrev_b32_e32 v5, 1, v8
	v_mul_lo_u32 v4, v10, s8
	v_mad_u64_u32 v[4:5], s[4:5], v5, s9, v[4:5]
	s_waitcnt vmcnt(6)
	v_or_b32_e32 v4, v4, v9
	v_add_lshl_u32 v140, v4, v11, 1
	v_or_b32_e32 v228, s24, v147
	v_mov_b32_e32 v139, v3
	v_mov_b32_e32 v141, v3
	s_mov_b32 s56, 0
	v_add_u32_e32 v149, 0, v22
	s_waitcnt lgkmcnt(0)
	s_barrier

;     __device__ bool next(int i, Unit& u) const { if (!base.next(i >> 1, u)) return false; if (i & 1) { u.pm += MTOK / BM; u.pn += DM / BM; } return true; }
; template <class Epi, class Sched, bool ALIGN_EPI = false, bool SP2 = false>
; __device__ __forceinline__ void gemm_phase(PG8_LAS unsigned char* lds, const Gemm g, const Sched& S, const Epi& E) {
;     ...
;     for (;;) {
;         const bool has_next = S.next(ui + 1, nxt);
;         const char* nA = has_next ? (const char*)g.A + (size_t)nxt.pm * tstep + (nxt.half == 2 ? hstep : (size_t)0) : cA; const char* nB = has_next ? (const char*)g.Bt + (size_t)nxt.pn * tstep : cB;
;         for (int t = 0; t < nt; t += 2) {
;             const bool last = (t == nt - 2);
;             const char* a1 = cA + (size_t)(t + 1) * kstep;
;             const char* a2 = last ? nA : cA + (size_t)(t + 2) * kstep; const char* b2 = last ? nB : cB + (size_t)(t + 2) * kstep;
;             const char* a3 = a2 + kstep; const char* b3 = b2 + kstep;
;             if (last && has_next) S.a_ready(nxt);
;             if constexpr (SP2) {
;             PG8_LDB(B0, 0, 0); PG8_LDB(B1, 0, 1); PG8_SCHED; PG8_LDA(At, 0, 0); PG8_STAGE(PG8_SA(1, 1), a1 + hstep, voffA);
;     ...
;             if (PROBE_KIND == 18 && t == 0 && ui > 0 && g.probe) { const unsigned long long tq_ = __builtin_amdgcn_s_memrealtime(); PG8_WAIT_V(8); pg8_probe_acc += (unsigned)(__builtin_amdgcn_s_memrealtime() - tq_); }
;     ...
;             PG8_WAIT_V(8); PG8_WAIT_L(0); PG8_BAR; PG8_MMA(0, 0, At, B0); PG8_MMA(0, 1, At, B1); PG8_BAR; PG8_SCHED;
;             PG8_LDA(At, 0, 1); PG8_STAGE(PG8_SB(0, 0), b2, voffB); PG8_STAGE(PG8_SB(0, 1), b2 + hstep, voffB); PG8_STAGE(PG8_SA(0, 0), a2, voffA);
;             PG8_WAIT_V(8); PG8_WAIT_L(0); PG8_BAR; if (cur.half == 0) { PG8_MMA(1, 0, At, B0); PG8_MMA(1, 1, At, B1); } PG8_BAR; PG8_SCHED;
;             PG8_LDB(B0, 1, 0); PG8_LDB(B1, 1, 1); PG8_SCHED; PG8_LDA(At, 1, 0); PG8_STAGE(PG8_SA(0, 1), a2 + hstep, voffA);
;             PG8_WAIT_V(8); PG8_WAIT_L(0); PG8_BAR; PG8_MMA(0, 0, At, B0); PG8_MMA(0, 1, At, B1); PG8_BAR; PG8_SCHED;
;             PG8_LDA(At, 1, 1); PG8_STAGE(PG8_SB(1, 0), b3, voffB); PG8_STAGE(PG8_SB(1, 1), b3 + hstep, voffB); PG8_STAGE(PG8_SA(1, 0), a3, voffA);
;             PG8_WAIT_V(8); PG8_WAIT_L(0); PG8_BAR; if (cur.half == 0) { PG8_MMA(1, 0, At, B0); PG8_MMA(1, 1, At, B1); } PG8_BAR; PG8_SCHED;
.LBB0_1779:
	s_add_u32 s60, s0, 0x100
	s_addc_u32 s61, s1, 0
	s_add_u32 s0, s6, 0xb0080
	s_addc_u32 s1, s7, 0
	v_lshl_add_u64 v[142:143], s[0:1], 0, v[138:139]
	v_lshl_add_u64 v[144:145], s[0:1], 0, v[140:141]
	s_mov_b32 s62, -2
	s_mov_b64 s[0:1], 0
	s_add_u32 s18, s6, s0
	s_addc_u32 s19, s7, s1
	s_add_u32 s18, s18, 0x100
	s_addc_u32 s19, s19, 0
	s_add_u32 s63, s60, s0
	s_addc_u32 s64, s61, s1
	s_add_i32 s65, 0, 0x10000
	s_cmpk_eq_i32 s0, 0x1500
	s_cselect_b32 s21, s15, s19
	s_cselect_b32 s20, s14, s18
	s_cselect_b32 s19, s11, s64
	s_cselect_b32 s18, s10, s63
	s_add_i32 s63, 0, 0x14000
	v_add_u32_e32 v162, s65, v148
	v_add_u32_e32 v178, s63, v148
	ds_read_b128 v[150:153], v162
	ds_read_b128 v[154:157], v162 offset:1024
	ds_read_b128 v[158:161], v162 offset:2048
	ds_read_b128 v[162:165], v162 offset:3072
	ds_read_b128 v[166:169], v178
	ds_read_b128 v[170:173], v178 offset:1024
	ds_read_b128 v[174:177], v178 offset:2048
	ds_read_b128 v[178:181], v178 offset:3072
	v_lshl_add_u64 v[214:215], v[142:143], 0, s[0:1]
	s_add_i32 m0, s35, 0xc000
	ds_read_b128 v[182:185], v149
	ds_read_b128 v[186:189], v149 offset:1024
	ds_read_b128 v[190:193], v149 offset:2048
	ds_read_b128 v[194:197], v149 offset:3072
	ds_read_b128 v[198:201], v149 offset:4096
	ds_read_b128 v[202:205], v149 offset:5120
	ds_read_b128 v[206:209], v149 offset:6144
	ds_read_b128 v[210:213], v149 offset:7168
	global_load_lds_dwordx4 v[214:215], off
	v_lshl_add_u64 v[214:215], v[144:145], 0, s[0:1]
	s_add_i32 m0, s35, 0xe000
	s_nop 0
	global_load_lds_dwordx4 v[214:215], off
	s_waitcnt vmcnt(8)
	s_waitcnt lgkmcnt(0)
	s_barrier
	s_setprio 1
	s_waitcnt lgkmcnt(0)
	v_mfma_f32_16x16x32_bf16 v[128:131], v[150:153], v[182:185], 0
	v_mfma_f32_16x16x32_bf16 v[124:127], v[158:161], v[182:185], 0
	v_mfma_f32_16x16x32_bf16 v[112:115], v[150:153], v[190:193], 0
	v_mfma_f32_16x16x32_bf16 v[108:111], v[158:161], v[190:193], 0
	v_mfma_f32_16x16x32_bf16 v[96:99], v[150:153], v[198:201], 0
	v_mfma_f32_16x16x32_bf16 v[92:95], v[158:161], v[198:201], 0
	v_mfma_f32_16x16x32_bf16 v[80:83], v[150:153], v[206:209], 0
	v_mfma_f32_16x16x32_bf16 v[76:79], v[158:161], v[206:209], 0
	v_mfma_f32_16x16x32_bf16 v[128:131], v[154:157], v[186:189], v[128:131]
	v_mfma_f32_16x16x32_bf16 v[124:127], v[162:165], v[186:189], v[124:127]
	v_mfma_f32_16x16x32_bf16 v[112:115], v[154:157], v[194:197], v[112:115]
	v_mfma_f32_16x16x32_bf16 v[108:111], v[162:165], v[194:197], v[108:111]
	v_mfma_f32_16x16x32_bf16 v[96:99], v[154:157], v[202:205], v[96:99]
	v_mfma_f32_16x16x32_bf16 v[92:95], v[162:165], v[202:205], v[92:95]
	v_mfma_f32_16x16x32_bf16 v[80:83], v[154:157], v[210:213], v[80:83]
	v_mfma_f32_16x16x32_bf16 v[76:79], v[162:165], v[210:213], v[76:79]
	s_setprio 0
	s_setprio 1
	v_mfma_f32_16x16x32_bf16 v[120:123], v[166:169], v[182:185], 0
	v_mfma_f32_16x16x32_bf16 v[116:119], v[174:177], v[182:185], 0
	v_mfma_f32_16x16x32_bf16 v[104:107], v[166:169], v[190:193], 0
	v_mfma_f32_16x16x32_bf16 v[100:103], v[174:177], v[190:193], 0
	v_mfma_f32_16x16x32_bf16 v[88:91], v[166:169], v[198:201], 0
	v_mfma_f32_16x16x32_bf16 v[84:87], v[174:177], v[198:201], 0
	v_mfma_f32_16x16x32_bf16 v[72:75], v[166:169], v[206:209], 0
	v_mfma_f32_16x16x32_bf16 v[68:71], v[174:177], v[206:209], 0
	v_mfma_f32_16x16x32_bf16 v[120:123], v[170:173], v[186:189], v[120:123]
	v_mfma_f32_16x16x32_bf16 v[116:119], v[178:181], v[186:189], v[116:119]
	v_mfma_f32_16x16x32_bf16 v[104:107], v[170:173], v[194:197], v[104:107]
	v_mfma_f32_16x16x32_bf16 v[100:103], v[178:181], v[194:197], v[100:103]
	v_mfma_f32_16x16x32_bf16 v[88:91], v[170:173], v[202:205], v[88:91]
	v_mfma_f32_16x16x32_bf16 v[84:87], v[178:181], v[202:205], v[84:87]
	v_mfma_f32_16x16x32_bf16 v[72:75], v[170:173], v[210:213], v[72:75]
	v_mfma_f32_16x16x32_bf16 v[68:71], v[178:181], v[210:213], v[68:71]
	s_setprio 0
	s_barrier
	s_add_i32 s64, s65, s34
	v_lshl_add_u64 v[214:215], s[18:19], 0, v[2:3]
	s_mov_b32 m0, s64
	ds_read_b128 v[182:185], v149 offset:16384
	ds_read_b128 v[186:189], v149 offset:17408
	ds_read_b128 v[190:193], v149 offset:18432
	ds_read_b128 v[194:197], v149 offset:19456
	ds_read_b128 v[198:201], v149 offset:20480
	ds_read_b128 v[202:205], v149 offset:21504
	ds_read_b128 v[206:209], v149 offset:22528
	ds_read_b128 v[210:213], v149 offset:23552
	global_load_lds_dwordx4 v[214:215], off
	s_add_i32 m0, s64, 0x2000
	s_add_u32 s64, s18, 0xb0000
	v_lshl_add_u64 v[216:217], s[18:19], 0, v[136:137]
	s_addc_u32 s65, s19, 0
	s_add_i32 s63, s63, s34
	global_load_lds_dwordx4 v[216:217], off
	v_lshl_add_u64 v[218:219], s[64:65], 0, v[2:3]
	s_mov_b32 m0, s63
	v_lshl_add_u64 v[220:221], s[20:21], 0, v[134:135]
	global_load_lds_dwordx4 v[218:219], off
	v_lshl_add_u64 v[218:219], s[64:65], 0, v[136:137]
	s_add_i32 m0, s63, 0x2000
	s_nop 0
	global_load_lds_dwordx4 v[218:219], off
	v_lshl_add_u64 v[218:219], s[20:21], 0, v[132:133]
	s_mov_b32 m0, s35
	s_nop 0
	global_load_lds_dwordx4 v[218:219], off
	s_mov_b32 m0, s36
	s_nop 0
	global_load_lds_dwordx4 v[220:221], off
	s_waitcnt vmcnt(8)
	s_waitcnt lgkmcnt(0)
	s_barrier
; #define PG8_STAGE(bufoff, gbase, voff) do { _Pragma("unroll") for (int _i = 0; _i < 2; ++_i) \
;         __builtin_amdgcn_global_load_lds((const unsigned*)((const char*)(gbase) + (voff)[_i]), (PG8_LAS unsigned*)(lds + (bufoff) + ldsw + _i * 8192), 16, 0, 0); } while (0)
; #define PG8_LDA(dst, b, h) do { _Pragma("unroll") for (int m = 0; m < 4; ++m) _Pragma("unroll") for (int k = 0; k < 2; ++k) dst[m][k] = *(const PG8_LAS bf16x8*)(lds + PG8_SA(b, h) + aoff + m * 2048 + k * 1024); } while (0)
; #define PG8_LDB(dst, b, h) do { _Pragma("unroll") for (int n = 0; n < 2; ++n) _Pragma("unroll") for (int k = 0; k < 2; ++k) dst[n][k] = *(const PG8_LAS bf16x8*)(lds + PG8_SB(b, h) + boff + n * 2048 + k * 1024); } while (0)
; #define PG8_WAIT_V(n) asm volatile("s_waitcnt vmcnt(" #n ")" ::: "memory")
; #define PG8_WAIT_L(n) asm volatile("s_waitcnt lgkmcnt(" #n ")" ::: "memory")
; template <class Epi, class Sched, bool ALIGN_EPI = false, bool SP2 = false>
; __device__ __forceinline__ void gemm_phase(PG8_LAS unsigned char* lds, const Gemm g, const Sched& S, const Epi& E) {
;     ...
;             PG8_LDB(B0, 0, 0); PG8_LDB(B1, 0, 1); PG8_SCHED; PG8_LDA(At, 0, 0); PG8_STAGE(PG8_SA(1, 1), a1 + hstep, voffA);
;     ...
;             if (PROBE_KIND == 18 && t == 0 && ui > 0 && g.probe) { const unsigned long long tq_ = __builtin_amdgcn_s_memrealtime(); PG8_WAIT_V(8); pg8_probe_acc += (unsigned)(__builtin_amdgcn_s_memrealtime() - tq_); }
;     ...
;             PG8_WAIT_V(8); PG8_WAIT_L(0); PG8_BAR; PG8_MMA(0, 0, At, B0); PG8_MMA(0, 1, At, B1); PG8_BAR; PG8_SCHED;
;             PG8_LDA(At, 0, 1); PG8_STAGE(PG8_SB(0, 0), b2, voffB); PG8_STAGE(PG8_SB(0, 1), b2 + hstep, voffB); PG8_STAGE(PG8_SA(0, 0), a2, voffA);
;             PG8_WAIT_V(8); PG8_WAIT_L(0); PG8_BAR; if (cur.half == 0) { PG8_MMA(1, 0, At, B0); PG8_MMA(1, 1, At, B1); } PG8_BAR; PG8_SCHED;
;             PG8_LDB(B0, 1, 0); PG8_LDB(B1, 1, 1); PG8_SCHED; PG8_LDA(At, 1, 0); PG8_STAGE(PG8_SA(0, 1), a2 + hstep, voffA);
;             PG8_WAIT_V(8); PG8_WAIT_L(0); PG8_BAR; PG8_MMA(0, 0, At, B0); PG8_MMA(0, 1, At, B1); PG8_BAR; PG8_SCHED;
;             PG8_LDA(At, 1, 1); PG8_STAGE(PG8_SB(1, 0), b3, voffB); PG8_STAGE(PG8_SB(1, 1), b3 + hstep, voffB); PG8_STAGE(PG8_SA(1, 0), a3, voffA);
;             PG8_WAIT_V(8); PG8_WAIT_L(0); PG8_BAR; if (cur.half == 0) { PG8_MMA(1, 0, At, B0); PG8_MMA(1, 1, At, B1); } PG8_BAR; PG8_SCHED;
	s_setprio 1
	s_waitcnt lgkmcnt(0)
	v_mfma_f32_16x16x32_bf16 v[64:67], v[150:153], v[182:185], 0
	v_mfma_f32_16x16x32_bf16 v[60:63], v[158:161], v[182:185], 0
	v_mfma_f32_16x16x32_bf16 v[48:51], v[150:153], v[190:193], 0
	v_mfma_f32_16x16x32_bf16 v[44:47], v[158:161], v[190:193], 0
	v_mfma_f32_16x16x32_bf16 v[32:35], v[150:153], v[198:201], 0
	v_mfma_f32_16x16x32_bf16 v[28:31], v[158:161], v[198:201], 0
	v_mfma_f32_16x16x32_bf16 v[16:19], v[150:153], v[206:209], 0
	v_mfma_f32_16x16x32_bf16 v[12:15], v[158:161], v[206:209], 0
	v_mfma_f32_16x16x32_bf16 v[64:67], v[154:157], v[186:189], v[64:67]
	v_mfma_f32_16x16x32_bf16 v[60:63], v[162:165], v[186:189], v[60:63]
	v_mfma_f32_16x16x32_bf16 v[48:51], v[154:157], v[194:197], v[48:51]
	v_mfma_f32_16x16x32_bf16 v[44:47], v[162:165], v[194:197], v[44:47]
	v_mfma_f32_16x16x32_bf16 v[32:35], v[154:157], v[202:205], v[32:35]
	v_mfma_f32_16x16x32_bf16 v[28:31], v[162:165], v[202:205], v[28:31]
	v_mfma_f32_16x16x32_bf16 v[16:19], v[154:157], v[210:213], v[16:19]
	v_mfma_f32_16x16x32_bf16 v[12:15], v[162:165], v[210:213], v[12:15]
	s_setprio 0
	s_setprio 1
	v_mfma_f32_16x16x32_bf16 v[56:59], v[166:169], v[182:185], 0
	v_mfma_f32_16x16x32_bf16 v[52:55], v[174:177], v[182:185], 0
	v_mfma_f32_16x16x32_bf16 v[40:43], v[166:169], v[190:193], 0
	v_mfma_f32_16x16x32_bf16 v[36:39], v[174:177], v[190:193], 0
	v_mfma_f32_16x16x32_bf16 v[24:27], v[166:169], v[198:201], 0
	v_mfma_f32_16x16x32_bf16 v[20:23], v[174:177], v[198:201], 0
	v_mfma_f32_16x16x32_bf16 v[8:11], v[166:169], v[206:209], 0
	v_mfma_f32_16x16x32_bf16 v[4:7], v[174:177], v[206:209], 0
	v_mfma_f32_16x16x32_bf16 v[56:59], v[170:173], v[186:189], v[56:59]
	v_mfma_f32_16x16x32_bf16 v[52:55], v[178:181], v[186:189], v[52:55]
	v_mfma_f32_16x16x32_bf16 v[40:43], v[170:173], v[194:197], v[40:43]
	v_mfma_f32_16x16x32_bf16 v[36:39], v[178:181], v[194:197], v[36:39]
	v_mfma_f32_16x16x32_bf16 v[24:27], v[170:173], v[202:205], v[24:27]
	v_mfma_f32_16x16x32_bf16 v[20:23], v[178:181], v[202:205], v[20:23]
	v_mfma_f32_16x16x32_bf16 v[8:11], v[170:173], v[210:213], v[8:11]
	v_mfma_f32_16x16x32_bf16 v[4:7], v[178:181], v[210:213], v[4:7]
	s_setprio 0
	s_barrier
	s_add_i32 s63, 0, 0x18000
	s_add_i32 s64, 0, 0x1c000
	v_add_u32_e32 v162, s63, v148
	v_add_u32_e32 v178, s64, v148
	ds_read_b128 v[150:153], v162
	ds_read_b128 v[154:157], v162 offset:1024
	ds_read_b128 v[158:161], v162 offset:2048
	ds_read_b128 v[162:165], v162 offset:3072
	ds_read_b128 v[166:169], v178
	ds_read_b128 v[170:173], v178 offset:1024
	ds_read_b128 v[174:177], v178 offset:2048
	ds_read_b128 v[178:181], v178 offset:3072
	s_add_u32 s20, s20, 0xb0000
	s_addc_u32 s21, s21, 0
	s_mov_b32 m0, s38
	v_lshl_add_u64 v[230:231], s[20:21], 0, v[132:133]
	ds_read_b128 v[182:185], v149 offset:32768
	ds_read_b128 v[186:189], v149 offset:33792
	ds_read_b128 v[190:193], v149 offset:34816
	ds_read_b128 v[194:197], v149 offset:35840
	ds_read_b128 v[198:201], v149 offset:36864
	ds_read_b128 v[202:205], v149 offset:37888
	ds_read_b128 v[206:209], v149 offset:38912
	ds_read_b128 v[210:213], v149 offset:39936
	global_load_lds_dwordx4 v[230:231], off
	v_lshl_add_u64 v[230:231], s[20:21], 0, v[134:135]
	s_mov_b32 m0, s39
	s_nop 0
	global_load_lds_dwordx4 v[230:231], off
	s_waitcnt vmcnt(8)
	s_waitcnt lgkmcnt(0)
	s_barrier
	s_setprio 1
	s_waitcnt lgkmcnt(0)
	v_mfma_f32_16x16x32_bf16 v[128:131], v[150:153], v[182:185], v[128:131]
	v_mfma_f32_16x16x32_bf16 v[124:127], v[158:161], v[182:185], v[124:127]
	v_mfma_f32_16x16x32_bf16 v[112:115], v[150:153], v[190:193], v[112:115]
	v_mfma_f32_16x16x32_bf16 v[108:111], v[158:161], v[190:193], v[108:111]
	v_mfma_f32_16x16x32_bf16 v[96:99], v[150:153], v[198:201], v[96:99]
	v_mfma_f32_16x16x32_bf16 v[92:95], v[158:161], v[198:201], v[92:95]
	v_mfma_f32_16x16x32_bf16 v[80:83], v[150:153], v[206:209], v[80:83]
	v_mfma_f32_16x16x32_bf16 v[76:79], v[158:161], v[206:209], v[76:79]
	v_mfma_f32_16x16x32_bf16 v[128:131], v[154:157], v[186:189], v[128:131]
	v_mfma_f32_16x16x32_bf16 v[124:127], v[162:165], v[186:189], v[124:127]
	v_mfma_f32_16x16x32_bf16 v[112:115], v[154:157], v[194:197], v[112:115]
	v_mfma_f32_16x16x32_bf16 v[108:111], v[162:165], v[194:197], v[108:111]
	v_mfma_f32_16x16x32_bf16 v[96:99], v[154:157], v[202:205], v[96:99]
	v_mfma_f32_16x16x32_bf16 v[92:95], v[162:165], v[202:205], v[92:95]
	v_mfma_f32_16x16x32_bf16 v[80:83], v[154:157], v[210:213], v[80:83]
	v_mfma_f32_16x16x32_bf16 v[76:79], v[162:165], v[210:213], v[76:79]
	s_setprio 0
	s_setprio 1
	v_mfma_f32_16x16x32_bf16 v[120:123], v[166:169], v[182:185], v[120:123]
	v_mfma_f32_16x16x32_bf16 v[116:119], v[174:177], v[182:185], v[116:119]
	v_mfma_f32_16x16x32_bf16 v[104:107], v[166:169], v[190:193], v[104:107]
	v_mfma_f32_16x16x32_bf16 v[100:103], v[174:177], v[190:193], v[100:103]
	v_mfma_f32_16x16x32_bf16 v[88:91], v[166:169], v[198:201], v[88:91]
	v_mfma_f32_16x16x32_bf16 v[84:87], v[174:177], v[198:201], v[84:87]
	v_mfma_f32_16x16x32_bf16 v[72:75], v[166:169], v[206:209], v[72:75]
	v_mfma_f32_16x16x32_bf16 v[68:71], v[174:177], v[206:209], v[68:71]
	v_mfma_f32_16x16x32_bf16 v[120:123], v[170:173], v[186:189], v[120:123]
	v_mfma_f32_16x16x32_bf16 v[116:119], v[178:181], v[186:189], v[116:119]
	v_mfma_f32_16x16x32_bf16 v[104:107], v[170:173], v[194:197], v[104:107]
	v_mfma_f32_16x16x32_bf16 v[100:103], v[178:181], v[194:197], v[100:103]
	v_mfma_f32_16x16x32_bf16 v[88:91], v[170:173], v[202:205], v[88:91]
	v_mfma_f32_16x16x32_bf16 v[84:87], v[178:181], v[202:205], v[84:87]
	v_mfma_f32_16x16x32_bf16 v[72:75], v[170:173], v[210:213], v[72:75]
	v_mfma_f32_16x16x32_bf16 v[68:71], v[178:181], v[210:213], v[68:71]
	s_setprio 0
	s_barrier
; #define PG8_STAGE(bufoff, gbase, voff) do { _Pragma("unroll") for (int _i = 0; _i < 2; ++_i) \
;         __builtin_amdgcn_global_load_lds((const unsigned*)((const char*)(gbase) + (voff)[_i]), (PG8_LAS unsigned*)(lds + (bufoff) + ldsw + _i * 8192), 16, 0, 0); } while (0)
; #define PG8_LDA(dst, b, h) do { _Pragma("unroll") for (int m = 0; m < 4; ++m) _Pragma("unroll") for (int k = 0; k < 2; ++k) dst[m][k] = *(const PG8_LAS bf16x8*)(lds + PG8_SA(b, h) + aoff + m * 2048 + k * 1024); } while (0)
; #define PG8_LDB(dst, b, h) do { _Pragma("unroll") for (int n = 0; n < 2; ++n) _Pragma("unroll") for (int k = 0; k < 2; ++k) dst[n][k] = *(const PG8_LAS bf16x8*)(lds + PG8_SB(b, h) + boff + n * 2048 + k * 1024); } while (0)
; #define PG8_WAIT_V(n) asm volatile("s_waitcnt vmcnt(" #n ")" ::: "memory")
; #define PG8_WAIT_L(n) asm volatile("s_waitcnt lgkmcnt(" #n ")" ::: "memory")
; template <class Epi, class Sched, bool ALIGN_EPI = false, bool SP2 = false>
; __device__ __forceinline__ void gemm_phase(PG8_LAS unsigned char* lds, const Gemm g, const Sched& S, const Epi& E) {
;     ...
;             PG8_LDB(B0, 0, 0); PG8_LDB(B1, 0, 1); PG8_SCHED; PG8_LDA(At, 0, 0); PG8_STAGE(PG8_SA(1, 1), a1 + hstep, voffA);
;     ...
;             if (PROBE_KIND == 18 && t == 0 && ui > 0 && g.probe) { const unsigned long long tq_ = __builtin_amdgcn_s_memrealtime(); PG8_WAIT_V(8); pg8_probe_acc += (unsigned)(__builtin_amdgcn_s_memrealtime() - tq_); }
;     ...
;             PG8_WAIT_V(8); PG8_WAIT_L(0); PG8_BAR; PG8_MMA(0, 0, At, B0); PG8_MMA(0, 1, At, B1); PG8_BAR; PG8_SCHED;
;             PG8_LDA(At, 0, 1); PG8_STAGE(PG8_SB(0, 0), b2, voffB); PG8_STAGE(PG8_SB(0, 1), b2 + hstep, voffB); PG8_STAGE(PG8_SA(0, 0), a2, voffA);
;             PG8_WAIT_V(8); PG8_WAIT_L(0); PG8_BAR; if (cur.half == 0) { PG8_MMA(1, 0, At, B0); PG8_MMA(1, 1, At, B1); } PG8_BAR; PG8_SCHED;
;             PG8_LDB(B0, 1, 0); PG8_LDB(B1, 1, 1); PG8_SCHED; PG8_LDA(At, 1, 0); PG8_STAGE(PG8_SA(0, 1), a2 + hstep, voffA);
;             PG8_WAIT_V(8); PG8_WAIT_L(0); PG8_BAR; PG8_MMA(0, 0, At, B0); PG8_MMA(0, 1, At, B1); PG8_BAR; PG8_SCHED;
;             PG8_LDA(At, 1, 1); PG8_STAGE(PG8_SB(1, 0), b3, voffB); PG8_STAGE(PG8_SB(1, 1), b3 + hstep, voffB); PG8_STAGE(PG8_SA(1, 0), a3, voffA);
;             PG8_WAIT_V(8); PG8_WAIT_L(0); PG8_BAR; if (cur.half == 0) { PG8_MMA(1, 0, At, B0); PG8_MMA(1, 1, At, B1); } PG8_BAR; PG8_SCHED;
	s_add_i32 s20, s63, s34
	v_lshl_add_u64 v[214:215], v[214:215], 0, s[42:43]
	s_mov_b32 m0, s20
	ds_read_b128 v[182:185], v149 offset:49152
	ds_read_b128 v[186:189], v149 offset:50176
	ds_read_b128 v[190:193], v149 offset:51200
	ds_read_b128 v[194:197], v149 offset:52224
	ds_read_b128 v[198:201], v149 offset:53248
	ds_read_b128 v[202:205], v149 offset:54272
	ds_read_b128 v[206:209], v149 offset:55296
	ds_read_b128 v[210:213], v149 offset:56320
	global_load_lds_dwordx4 v[214:215], off
	s_add_i32 m0, s20, 0x2000
	s_add_u32 s18, s18, 0xb0080
	v_lshl_add_u64 v[214:215], v[216:217], 0, s[42:43]
	s_addc_u32 s19, s19, 0
	s_add_i32 s20, s64, s34
	global_load_lds_dwordx4 v[214:215], off
	v_lshl_add_u64 v[214:215], s[18:19], 0, v[2:3]
	s_mov_b32 m0, s20
	s_nop 0
	global_load_lds_dwordx4 v[214:215], off
	v_lshl_add_u64 v[214:215], s[18:19], 0, v[136:137]
	s_add_i32 m0, s20, 0x2000
	s_nop 0
	global_load_lds_dwordx4 v[214:215], off
	v_lshl_add_u64 v[214:215], v[218:219], 0, s[42:43]
	s_mov_b32 m0, s40
	s_nop 0
	global_load_lds_dwordx4 v[214:215], off
	v_lshl_add_u64 v[214:215], v[220:221], 0, s[42:43]
	s_mov_b32 m0, s41
	s_nop 0
	global_load_lds_dwordx4 v[214:215], off
	s_waitcnt vmcnt(8)
	s_waitcnt lgkmcnt(0)
	s_barrier
	s_setprio 1
	s_waitcnt lgkmcnt(0)
	v_mfma_f32_16x16x32_bf16 v[64:67], v[150:153], v[182:185], v[64:67]
	v_mfma_f32_16x16x32_bf16 v[60:63], v[158:161], v[182:185], v[60:63]
	v_mfma_f32_16x16x32_bf16 v[48:51], v[150:153], v[190:193], v[48:51]
	v_mfma_f32_16x16x32_bf16 v[44:47], v[158:161], v[190:193], v[44:47]
	v_mfma_f32_16x16x32_bf16 v[32:35], v[150:153], v[198:201], v[32:35]
	v_mfma_f32_16x16x32_bf16 v[28:31], v[158:161], v[198:201], v[28:31]
	v_mfma_f32_16x16x32_bf16 v[16:19], v[150:153], v[206:209], v[16:19]
	v_mfma_f32_16x16x32_bf16 v[12:15], v[158:161], v[206:209], v[12:15]
	v_mfma_f32_16x16x32_bf16 v[64:67], v[154:157], v[186:189], v[64:67]
	v_mfma_f32_16x16x32_bf16 v[60:63], v[162:165], v[186:189], v[60:63]
	v_mfma_f32_16x16x32_bf16 v[48:51], v[154:157], v[194:197], v[48:51]
	v_mfma_f32_16x16x32_bf16 v[44:47], v[162:165], v[194:197], v[44:47]
	v_mfma_f32_16x16x32_bf16 v[32:35], v[154:157], v[202:205], v[32:35]
	v_mfma_f32_16x16x32_bf16 v[28:31], v[162:165], v[202:205], v[28:31]
	v_mfma_f32_16x16x32_bf16 v[16:19], v[154:157], v[210:213], v[16:19]
	v_mfma_f32_16x16x32_bf16 v[12:15], v[162:165], v[210:213], v[12:15]
	s_setprio 0
	s_setprio 1
	v_mfma_f32_16x16x32_bf16 v[56:59], v[166:169], v[182:185], v[56:59]
	v_mfma_f32_16x16x32_bf16 v[52:55], v[174:177], v[182:185], v[52:55]
	v_mfma_f32_16x16x32_bf16 v[40:43], v[166:169], v[190:193], v[40:43]
	v_mfma_f32_16x16x32_bf16 v[36:39], v[174:177], v[190:193], v[36:39]
	v_mfma_f32_16x16x32_bf16 v[24:27], v[166:169], v[198:201], v[24:27]
	v_mfma_f32_16x16x32_bf16 v[20:23], v[174:177], v[198:201], v[20:23]
	v_mfma_f32_16x16x32_bf16 v[8:11], v[166:169], v[206:209], v[8:11]
	v_mfma_f32_16x16x32_bf16 v[4:7], v[174:177], v[206:209], v[4:7]
	v_mfma_f32_16x16x32_bf16 v[56:59], v[170:173], v[186:189], v[56:59]
	v_mfma_f32_16x16x32_bf16 v[52:55], v[178:181], v[186:189], v[52:55]
	v_mfma_f32_16x16x32_bf16 v[40:43], v[170:173], v[194:197], v[40:43]
	v_mfma_f32_16x16x32_bf16 v[36:39], v[178:181], v[194:197], v[36:39]
	v_mfma_f32_16x16x32_bf16 v[24:27], v[170:173], v[202:205], v[24:27]
	v_mfma_f32_16x16x32_bf16 v[20:23], v[178:181], v[202:205], v[20:23]
	v_mfma_f32_16x16x32_bf16 v[8:11], v[170:173], v[210:213], v[8:11]
	v_mfma_f32_16x16x32_bf16 v[4:7], v[178:181], v[210:213], v[4:7]
	s_setprio 0
	s_barrier
	s_add_i32 s62, s62, 2
	s_add_u32 s0, s0, 0x100
	s_addc_u32 s1, s1, 0
